# speedup vs baseline: 1.0000x; 1.0000x over previous
_Z11attn_kernelPKDF16_S0_S0_PDF16_:
	v_readfirstlane_b32 s50, v0
	s_bfe_u32 s52, s50, 0x10006
	s_lshr_b32 s50, s50, 7
	s_and_b32 s6, s2, 3
	s_cmpk_gt_u32 s2, 0xdf
	s_mul_i32 s6, s6, 7
	s_cbranch_scc0 .LBB1_2
	s_lshr_b32 s3, s2, 3
	s_sub_i32 s4, s3, 28
	s_lshl_b32 s3, s4, 1
	s_add_i32 s3, s3, s6
	s_add_i32 s28, s3, 1
	s_cmp_eq_u32 s4, 3
	s_cselect_b32 s30, -1, 3
	s_movk_i32 s14, 0x300
	s_cbranch_execz .LBB1_3
	s_branch .LBB1_4

.LBB1_27:
	s_add_i32 s25, s45, s24
	s_add_i32 s2, s44, s40
	s_add_i32 s3, s25, 2
	s_mov_b32 s51, s3
	s_cmp_lt_i32 s3, s50
	s_mov_b32 s3, m0
	s_mov_b32 m0, s2
	s_nop 0
	global_load_lds_dwordx4 v211, s[18:19]
	s_mov_b32 m0, s3
	s_cbranch_scc1 .LBB1_29
	s_cmp_gt_i32 s51, s50
	s_cbranch_scc1 .Lmfill_0a
	s_cmp_lg_u32 s52, 0
	s_cbranch_scc1 .Lpodd_0a
	s_nop 7
	s_nop 3
	v_add_u32_e32 v59, 0xffffff85, v201
	v_cmp_lt_i32_e64 s[54:55], v59, v204
	v_add_u32_e32 v60, 0xffffff85, v201
	v_cmp_le_i32_e64 s[56:57], v60, v204
	v_add_u32_e32 v59, 0xffffff87, v201
	v_cmp_le_i32_e64 s[58:59], v59, v204
	v_cndmask_b32_e64 v99, v205, v99, s[54:55]
	v_add_u32_e32 v60, 0xffffff88, v201
	v_cmp_le_i32_e64 s[54:55], v60, v204
	v_cndmask_b32_e64 v98, v205, v98, s[56:57]
	v_add_u32_e32 v59, 0xffffff8d, v201
	v_cmp_le_i32_e64 s[56:57], v59, v204
	v_cndmask_b32_e64 v100, v205, v100, s[58:59]
	v_add_u32_e32 v60, 0xffffff8e, v201
	v_cmp_le_i32_e64 s[58:59], v60, v204
	v_cndmask_b32_e64 v101, v205, v101, s[54:55]
	v_add_u32_e32 v59, 0xffffff8f, v201
	v_cmp_le_i32_e64 s[54:55], v59, v204
	v_cndmask_b32_e64 v102, v205, v102, s[56:57]
	v_add_u32_e32 v60, 0xffffff90, v201
	v_cmp_le_i32_e64 s[56:57], v60, v204
	v_cndmask_b32_e64 v103, v205, v103, s[58:59]
	v_add_u32_e32 v59, 0xffffff95, v201
	v_cmp_le_i32_e64 s[58:59], v59, v204
	v_cndmask_b32_e64 v104, v205, v104, s[54:55]
	v_add_u32_e32 v60, 0xffffff96, v201
	v_cmp_le_i32_e64 s[54:55], v60, v204
	v_cndmask_b32_e64 v105, v205, v105, s[56:57]
	v_add_u32_e32 v59, 0xffffff97, v201
	v_cmp_le_i32_e64 s[56:57], v59, v204
	v_cndmask_b32_e64 v106, v205, v106, s[58:59]
	v_add_u32_e32 v60, 0xffffff98, v201
	v_cmp_le_i32_e64 s[58:59], v60, v204
	v_cndmask_b32_e64 v107, v205, v107, s[54:55]
	v_add_u32_e32 v59, 0xffffff9d, v201
	v_cmp_le_i32_e64 s[54:55], v59, v204
	v_cndmask_b32_e64 v108, v205, v108, s[56:57]
	v_add_u32_e32 v60, 0xffffff9e, v201
	v_cmp_le_i32_e64 s[56:57], v60, v204
	v_cndmask_b32_e64 v109, v205, v109, s[58:59]
	v_add_u32_e32 v59, 0xffffff9f, v201
	v_cmp_le_i32_e64 s[58:59], v59, v204
	v_cndmask_b32_e64 v110, v205, v110, s[54:55]
	v_add_u32_e32 v60, 0xffffffa0, v201
	v_cmp_le_i32_e64 s[54:55], v60, v204
	v_cndmask_b32_e64 v111, v205, v111, s[56:57]
	v_cndmask_b32_e64 v112, v205, v112, s[58:59]
	v_cndmask_b32_e64 v113, v205, v113, s[54:55]
	v_mov_b32_e32 v82, v205
	v_mov_b32_e32 v83, v205
	v_mov_b32_e32 v84, v205
	v_mov_b32_e32 v85, v205
	v_mov_b32_e32 v86, v205
	v_mov_b32_e32 v87, v205
	v_mov_b32_e32 v88, v205
	v_mov_b32_e32 v89, v205
	v_mov_b32_e32 v90, v205
	v_mov_b32_e32 v91, v205
	v_mov_b32_e32 v92, v205
	v_mov_b32_e32 v93, v205
	v_mov_b32_e32 v94, v205
	v_mov_b32_e32 v95, v205
	v_mov_b32_e32 v96, v205
	v_mov_b32_e32 v97, v205
	s_branch .Lpend_0a
.Lpodd_0a:
	s_nop 7
	s_nop 3
	v_add_u32_e32 v59, 0xffffffa5, v201
	v_cmp_le_i32_e64 s[54:55], v59, v204
	v_add_u32_e32 v60, 0xffffffa6, v201
	v_cmp_le_i32_e64 s[56:57], v60, v204
	v_add_u32_e32 v59, 0xffffffa7, v201
	v_cmp_le_i32_e64 s[58:59], v59, v204
	v_cndmask_b32_e64 v82, v205, v82, s[54:55]
	v_add_u32_e32 v60, 0xffffffa8, v201
	v_cmp_le_i32_e64 s[54:55], v60, v204
	v_cndmask_b32_e64 v83, v205, v83, s[56:57]
	v_add_u32_e32 v59, 0xffffffad, v201
	v_cmp_le_i32_e64 s[56:57], v59, v204
	v_cndmask_b32_e64 v84, v205, v84, s[58:59]
	v_add_u32_e32 v60, 0xffffffae, v201
	v_cmp_le_i32_e64 s[58:59], v60, v204
	v_cndmask_b32_e64 v85, v205, v85, s[54:55]
	v_add_u32_e32 v59, 0xffffffaf, v201
	v_cmp_le_i32_e64 s[54:55], v59, v204
	v_cndmask_b32_e64 v86, v205, v86, s[56:57]
	v_add_u32_e32 v60, 0xffffffb0, v201
	v_cmp_le_i32_e64 s[56:57], v60, v204
	v_cndmask_b32_e64 v87, v205, v87, s[58:59]
	v_add_u32_e32 v59, 0xffffffb5, v201
	v_cmp_le_i32_e64 s[58:59], v59, v204
	v_cndmask_b32_e64 v88, v205, v88, s[54:55]
	v_add_u32_e32 v60, 0xffffffb6, v201
	v_cmp_le_i32_e64 s[54:55], v60, v204
	v_cndmask_b32_e64 v89, v205, v89, s[56:57]
	v_add_u32_e32 v59, 0xffffffb7, v201
	v_cmp_le_i32_e64 s[56:57], v59, v204
	v_cndmask_b32_e64 v90, v205, v90, s[58:59]
	v_add_u32_e32 v60, 0xffffffb8, v201
	v_cmp_le_i32_e64 s[58:59], v60, v204
	v_cndmask_b32_e64 v91, v205, v91, s[54:55]
	v_add_u32_e32 v59, 0xffffffbd, v201
	v_cmp_le_i32_e64 s[54:55], v59, v204
	v_cndmask_b32_e64 v92, v205, v92, s[56:57]
	v_add_u32_e32 v60, 0xffffffbe, v201
	v_cmp_le_i32_e64 s[56:57], v60, v204
	v_cndmask_b32_e64 v93, v205, v93, s[58:59]
	v_add_u32_e32 v59, 0xffffffbf, v201
	v_cmp_le_i32_e64 s[58:59], v59, v204
	v_cndmask_b32_e64 v94, v205, v94, s[54:55]
	v_subrev_u32_e32 v60, 64, v201
	v_cmp_le_i32_e64 s[54:55], v60, v204
	v_cndmask_b32_e64 v95, v205, v95, s[56:57]
	v_cndmask_b32_e64 v96, v205, v96, s[58:59]
	v_cndmask_b32_e64 v97, v205, v97, s[54:55]
.Lpend_0a:
.LBB1_29:
	v_add_f32_e32 v203, v203, v58
	v_max_f32_e32 v58, v99, v99
	v_max_f32_e32 v59, v98, v98
	v_max_f32_e32 v58, v59, v58
	v_max3_f32 v59, v100, v101, v83
	v_max3_f32 v58, v58, v82, v84
	v_max3_f32 v58, v58, v85, v102
	v_max3_f32 v59, v59, v104, v105
	v_max3_f32 v58, v58, v103, v86
	v_max3_f32 v59, v59, v88, v89
	v_max3_f32 v58, v58, v87, v106
	v_max3_f32 v59, v59, v108, v109
	v_max3_f32 v58, v58, v107, v90
	v_max3_f32 v59, v59, v92, v93
	v_max3_f32 v58, v58, v91, v110
	v_max3_f32 v59, v59, v112, v113
	v_max3_f32 v58, v58, v111, v94
	v_max3_f32 v59, v59, v96, v97
	v_max3_f32 v58, v58, v95, v59
	v_mov_b32_e32 v59, v58
	s_nop 1
	v_permlane32_swap_b32_e32 v58, v59
	v_max_f32_e32 v59, v59, v59
	v_max_f32_e32 v58, v58, v58
	v_max_f32_e32 v58, v58, v59
	v_cmp_lt_f32_e32 vcc, s46, v58
	s_cmp_lg_u64 vcc, 0
	s_cselect_b64 s[2:3], -1, 0
	s_cbranch_vccnz .LBB1_67

.LBB1_38:
	s_add_i32 s25, s25, 3
	s_cmp_lt_i32 s25, s50
	s_cbranch_scc1 .LBB1_40
	s_cmp_gt_i32 s25, s50
	s_cbranch_scc1 .Lmfill_0b
	s_cmp_lg_u32 s52, 0
	s_cbranch_scc1 .Lpodd_0b
	s_nop 7
	s_nop 3
	v_subrev_u32_e32 v91, 59, v201
	v_cmp_lt_u32_e64 s[54:55], v91, v204
	v_subrev_u32_e32 v92, 59, v201
	v_cmp_le_u32_e64 s[56:57], v92, v204
	v_subrev_u32_e32 v91, 57, v201
	v_cmp_le_u32_e64 s[58:59], v91, v204
	v_cndmask_b32_e64 v67, v205, v67, s[54:55]
	v_subrev_u32_e32 v92, 56, v201
	v_cmp_le_u32_e64 s[54:55], v92, v204
	v_cndmask_b32_e64 v66, v205, v66, s[56:57]
	v_subrev_u32_e32 v91, 51, v201
	v_cmp_le_u32_e64 s[56:57], v91, v204
	v_cndmask_b32_e64 v68, v205, v68, s[58:59]
	v_subrev_u32_e32 v92, 50, v201
	v_cmp_le_u32_e64 s[58:59], v92, v204
	v_cndmask_b32_e64 v69, v205, v69, s[54:55]
	v_subrev_u32_e32 v91, 49, v201
	v_cmp_le_u32_e64 s[54:55], v91, v204
	v_cndmask_b32_e64 v70, v205, v70, s[56:57]
	v_subrev_u32_e32 v92, 48, v201
	v_cmp_le_u32_e64 s[56:57], v92, v204
	v_cndmask_b32_e64 v71, v205, v71, s[58:59]
	v_subrev_u32_e32 v91, 43, v201
	v_cmp_le_u32_e64 s[58:59], v91, v204
	v_cndmask_b32_e64 v72, v205, v72, s[54:55]
	v_subrev_u32_e32 v92, 42, v201
	v_cmp_le_u32_e64 s[54:55], v92, v204
	v_cndmask_b32_e64 v73, v205, v73, s[56:57]
	v_subrev_u32_e32 v91, 41, v201
	v_cmp_le_u32_e64 s[56:57], v91, v204
	v_cndmask_b32_e64 v74, v205, v74, s[58:59]
	v_subrev_u32_e32 v92, 40, v201
	v_cmp_le_u32_e64 s[58:59], v92, v204
	v_cndmask_b32_e64 v75, v205, v75, s[54:55]
	v_subrev_u32_e32 v91, 35, v201
	v_cmp_le_u32_e64 s[54:55], v91, v204
	v_cndmask_b32_e64 v76, v205, v76, s[56:57]
	v_subrev_u32_e32 v92, 34, v201
	v_cmp_le_u32_e64 s[56:57], v92, v204
	v_cndmask_b32_e64 v77, v205, v77, s[58:59]
	v_subrev_u32_e32 v91, 33, v201
	v_cmp_le_u32_e64 s[58:59], v91, v204
	v_cndmask_b32_e64 v78, v205, v78, s[54:55]
	v_subrev_u32_e32 v92, 32, v201
	v_cmp_le_u32_e64 s[54:55], v92, v204
	v_cndmask_b32_e64 v79, v205, v79, s[56:57]
	v_cndmask_b32_e64 v80, v205, v80, s[58:59]
	v_cndmask_b32_e64 v81, v205, v81, s[54:55]
	v_mov_b32_e32 v50, v205
	v_mov_b32_e32 v51, v205
	v_mov_b32_e32 v52, v205
	v_mov_b32_e32 v53, v205
	v_mov_b32_e32 v54, v205
	v_mov_b32_e32 v55, v205
	v_mov_b32_e32 v56, v205
	v_mov_b32_e32 v57, v205
	v_mov_b32_e32 v58, v205
	v_mov_b32_e32 v59, v205
	v_mov_b32_e32 v60, v205
	v_mov_b32_e32 v61, v205
	v_mov_b32_e32 v62, v205
	v_mov_b32_e32 v63, v205
	v_mov_b32_e32 v64, v205
	v_mov_b32_e32 v65, v205
	s_branch .Lpend_0b
.Lpodd_0b:
	s_nop 7
	s_nop 3
	v_subrev_u32_e32 v91, 27, v201
	v_cmp_le_u32_e64 s[54:55], v91, v204
	v_subrev_u32_e32 v92, 26, v201
	v_cmp_le_u32_e64 s[56:57], v92, v204
	v_subrev_u32_e32 v91, 25, v201
	v_cmp_le_u32_e64 s[58:59], v91, v204
	v_cndmask_b32_e64 v50, v205, v50, s[54:55]
	v_subrev_u32_e32 v92, 24, v201
	v_cmp_le_u32_e64 s[54:55], v92, v204
	v_cndmask_b32_e64 v51, v205, v51, s[56:57]
	v_subrev_u32_e32 v91, 19, v201
	v_cmp_le_u32_e64 s[56:57], v91, v204
	v_cndmask_b32_e64 v52, v205, v52, s[58:59]
	v_subrev_u32_e32 v92, 18, v201
	v_cmp_le_u32_e64 s[58:59], v92, v204
	v_cndmask_b32_e64 v53, v205, v53, s[54:55]
	v_subrev_u32_e32 v91, 17, v201
	v_cmp_le_u32_e64 s[54:55], v91, v204
	v_cndmask_b32_e64 v54, v205, v54, s[56:57]
	v_add_u32_e32 v92, -16, v201
	v_cmp_le_u32_e64 s[56:57], v92, v204
	v_cndmask_b32_e64 v55, v205, v55, s[58:59]
	v_add_u32_e32 v91, -11, v201
	v_cmp_le_u32_e64 s[58:59], v91, v204
	v_cndmask_b32_e64 v56, v205, v56, s[54:55]
	v_add_u32_e32 v92, -10, v201
	v_cmp_le_u32_e64 s[54:55], v92, v204
	v_cndmask_b32_e64 v57, v205, v57, s[56:57]
	v_add_u32_e32 v91, -9, v201
	v_cmp_le_u32_e64 s[56:57], v91, v204
	v_cndmask_b32_e64 v58, v205, v58, s[58:59]
	v_add_u32_e32 v92, -8, v201
	v_cmp_le_u32_e64 s[58:59], v92, v204
	v_cndmask_b32_e64 v59, v205, v59, s[54:55]
	v_add_u32_e32 v91, -3, v201
	v_cmp_le_u32_e64 s[54:55], v91, v204
	v_cndmask_b32_e64 v60, v205, v60, s[56:57]
	v_add_u32_e32 v92, -2, v201
	v_cmp_le_u32_e64 s[56:57], v92, v204
	v_cndmask_b32_e64 v61, v205, v61, s[58:59]
	v_add_u32_e32 v91, -1, v201
	v_cmp_le_u32_e64 s[58:59], v91, v204
	v_cndmask_b32_e64 v62, v205, v62, s[54:55]
	v_cmp_le_u32_e64 s[54:55], v201, v204
	v_cndmask_b32_e64 v63, v205, v63, s[56:57]
	v_cndmask_b32_e64 v64, v205, v64, s[58:59]
	v_cndmask_b32_e64 v65, v205, v65, s[54:55]
.Lpend_0b:
.LBB1_40:
	v_add_f32_e32 v203, v203, v90
	v_max_f32_e32 v90, v67, v67
	v_max_f32_e32 v91, v66, v66
	v_max_f32_e32 v90, v91, v90
	v_max3_f32 v91, v68, v69, v51
	v_max3_f32 v90, v90, v50, v52
	v_max3_f32 v90, v90, v53, v70
	v_max3_f32 v91, v91, v72, v73
	v_max3_f32 v90, v90, v71, v54
	v_max3_f32 v91, v91, v56, v57
	v_max3_f32 v90, v90, v55, v74
	v_max3_f32 v91, v91, v76, v77
	v_max3_f32 v90, v90, v75, v58
	v_max3_f32 v91, v91, v60, v61
	v_max3_f32 v90, v90, v59, v78
	v_max3_f32 v91, v91, v80, v81
	v_max3_f32 v90, v90, v79, v62
	v_max3_f32 v91, v91, v64, v65
	v_max3_f32 v90, v90, v63, v91
	v_mov_b32_e32 v91, v90
	s_nop 1
	v_permlane32_swap_b32_e32 v90, v91
	v_max_f32_e32 v91, v91, v91
	v_max_f32_e32 v90, v90, v90
	v_max_f32_e32 v90, v90, v91
	v_cmp_lt_f32_e32 vcc, s46, v90
	s_cmp_lg_u64 vcc, 0
	s_cselect_b64 s[24:25], -1, 0
	s_cbranch_vccnz .LBB1_70

.LBB1_74:
	v_add_u32_e32 v100, s44, v209
	ds_read_b64_tr_b16 v[178:179], v100 offset:24576
	ds_read_b64_tr_b16 v[180:181], v100 offset:25088
	v_add_f32_e32 v82, v66, v67
	v_add_f32_e32 v82, v68, v82
	v_add_f32_e32 v82, v69, v82
	v_add_f32_e32 v82, v70, v82
	v_add_f32_e32 v98, v71, v82
	s_waitcnt lgkmcnt(9)
	v_mfma_f32_32x32x16_f16 v[82:97], v[174:177], v[142:145], v[34:49]
	v_cvt_pk_f16_f32 v134, v66, v67
	v_cvt_pk_f16_f32 v135, v68, v69
	ds_read_b64_tr_b16 v[174:175], v100 offset:28672
	ds_read_b64_tr_b16 v[176:177], v100 offset:29184
	s_waitcnt lgkmcnt(10)
	v_mfma_f32_32x32x16_f16 v[34:49], v[170:173], v[142:145], v[34:49]
	v_add_f32_e32 v66, v72, v98
	v_add_f32_e32 v66, v73, v66
	v_add_f32_e32 v66, v74, v66
	v_add_f32_e32 v66, v75, v66
	v_cvt_pk_f16_f32 v136, v70, v71
	v_cvt_pk_f16_f32 v137, v72, v73
	ds_read_b64_tr_b16 v[170:171], v100 offset:25600
	ds_read_b64_tr_b16 v[172:173], v100 offset:26112
	s_waitcnt lgkmcnt(11)
	v_mfma_f32_32x32x16_f16 v[82:97], v[166:169], v[138:141], v[82:97]
	v_add_f32_e32 v66, v76, v66
	v_add_f32_e32 v66, v77, v66
	v_add_f32_e32 v66, v78, v66
	v_add_f32_e32 v66, v79, v66
	v_cvt_pk_f16_f32 v126, v74, v75
	v_cvt_pk_f16_f32 v127, v76, v77
	ds_read_b64_tr_b16 v[142:143], v100 offset:29696
	ds_read_b64_tr_b16 v[144:145], v100 offset:30208
	s_waitcnt lgkmcnt(12)
	v_mfma_f32_32x32x16_f16 v[34:49], v[162:165], v[138:141], v[34:49]
	v_add_f32_e32 v66, v80, v66
	v_add_f32_e32 v66, v81, v66
	v_add_f32_e32 v66, v50, v66
	v_add_f32_e32 v66, v51, v66
	v_cvt_pk_f16_f32 v128, v78, v79
	v_cvt_pk_f16_f32 v129, v80, v81
	ds_read_b64_tr_b16 v[110:111], v100 offset:26624
	ds_read_b64_tr_b16 v[112:113], v100 offset:27136
	s_waitcnt lgkmcnt(13)
	v_mfma_f32_32x32x16_f16 v[82:97], v[158:161], v[130:133], v[82:97]
	v_add_f32_e32 v66, v52, v66
	v_add_f32_e32 v66, v53, v66
	v_add_f32_e32 v66, v54, v66
	v_add_f32_e32 v66, v55, v66
	v_cvt_pk_f16_f32 v118, v50, v51
	v_cvt_pk_f16_f32 v119, v52, v53
	ds_read_b64_tr_b16 v[106:107], v100 offset:30720
	ds_read_b64_tr_b16 v[108:109], v100 offset:31232
	s_waitcnt lgkmcnt(14)
	v_mfma_f32_32x32x16_f16 v[34:49], v[154:157], v[130:133], v[34:49]
	v_add_f32_e32 v50, v56, v66
	v_add_f32_e32 v50, v57, v50
	v_add_f32_e32 v50, v58, v50
	v_add_f32_e32 v50, v59, v50
	v_cvt_pk_f16_f32 v120, v54, v55
	v_cvt_pk_f16_f32 v121, v56, v57
	ds_read_b64_tr_b16 v[102:103], v100 offset:27648
	ds_read_b64_tr_b16 v[104:105], v100 offset:28160
	s_waitcnt lgkmcnt(14)
	v_mfma_f32_32x32x16_f16 v[82:97], v[150:153], v[122:125], v[82:97]
	v_add_f32_e32 v50, v60, v50
	v_add_f32_e32 v50, v61, v50
	v_add_f32_e32 v50, v62, v50
	v_add_f32_e32 v50, v63, v50
	v_cvt_pk_f16_f32 v114, v58, v59
	v_cvt_pk_f16_f32 v115, v60, v61
	ds_read_b64_tr_b16 v[98:99], v100 offset:31744
	ds_read_b64_tr_b16 v[100:101], v100 offset:32256
	v_mfma_f32_32x32x16_f16 v[34:49], v[146:149], v[122:125], v[34:49]
	v_add_f32_e32 v50, v64, v50
	v_add_f32_e32 v50, v65, v50
	v_add_f32_e32 v66, 0, v50
	v_cvt_pk_f16_f32 v116, v62, v63
	v_cvt_pk_f16_f32 v117, v64, v65
	s_cmp_lt_u32 s50, 3
	s_cbranch_scc1 .Lmfill_0f
	s_cmp_lg_u32 s52, 0
	s_cbranch_scc1 .Lpodd_0f
	s_nop 7
	s_nop 3
	v_mov_b32_e32 v67, 0xff800000
	v_or_b32_e32 v214, 0xe0, v210
	v_or_b32_e32 v213, 0xc0, v210
	v_or_b32_e32 v215, 0xe1, v210
	v_or_b32_e32 v216, 0xc2, v210
	v_or_b32_e32 v217, 0xe2, v210
	v_or_b32_e32 v218, 0xc3, v210
	v_or_b32_e32 v219, 0xe3, v210
	v_or_b32_e32 v220, 0xc8, v210
	v_or_b32_e32 v221, 0xe8, v210
	v_or_b32_e32 v222, 0xc9, v210
	v_or_b32_e32 v223, 0xe9, v210
	v_or_b32_e32 v224, 0xca, v210
	v_or_b32_e32 v225, 0xea, v210
	v_or_b32_e32 v226, 0xcb, v210
	v_or_b32_e32 v227, 0xeb, v210
	v_or_b32_e32 v228, 0xd0, v210
	v_or_b32_e32 v229, 0xf0, v210
	v_or_b32_e32 v230, 0xd1, v210
	v_or_b32_e32 v231, 0xf1, v210
	v_or_b32_e32 v232, 0xd2, v210
	v_or_b32_e32 v233, 0xf2, v210
	v_or_b32_e32 v234, 0xd3, v210
	v_or_b32_e32 v235, 0xf3, v210
	v_or_b32_e32 v236, 0xd8, v210
	v_or_b32_e32 v237, 0xf8, v210
	v_or_b32_e32 v238, 0xd9, v210
	v_or_b32_e32 v239, 0xf9, v210
	v_or_b32_e32 v240, 0xda, v210
	v_or_b32_e32 v241, 0xfa, v210
	v_or_b32_e32 v242, 0xdb, v210
	v_or_b32_e32 v243, 0xfb, v210
	v_cmp_lt_u32_e64 s[54:55], v213, v204
	v_cmp_le_u32_e64 s[56:57], v213, v204
	v_cmp_le_u32_e64 s[58:59], v216, v204
	v_cndmask_b32_e64 v51, v67, v83, s[54:55]
	v_cmp_le_u32_e64 s[54:55], v218, v204
	v_cndmask_b32_e64 v50, v67, v82, s[56:57]
	v_cmp_le_u32_e64 s[56:57], v220, v204
	v_cndmask_b32_e64 v52, v67, v84, s[58:59]
	v_cmp_le_u32_e64 s[58:59], v222, v204
	v_cndmask_b32_e64 v53, v67, v85, s[54:55]
	v_cmp_le_u32_e64 s[54:55], v224, v204
	v_cndmask_b32_e64 v54, v67, v86, s[56:57]
	v_cmp_le_u32_e64 s[56:57], v226, v204
	v_cndmask_b32_e64 v55, v67, v87, s[58:59]
	v_cmp_le_u32_e64 s[58:59], v228, v204
	v_cndmask_b32_e64 v56, v67, v88, s[54:55]
	v_cmp_le_u32_e64 s[54:55], v230, v204
	v_cndmask_b32_e64 v57, v67, v89, s[56:57]
	v_cmp_le_u32_e64 s[56:57], v232, v204
	v_cndmask_b32_e64 v58, v67, v90, s[58:59]
	v_cmp_le_u32_e64 s[58:59], v234, v204
	v_cndmask_b32_e64 v59, v67, v91, s[54:55]
	v_cmp_le_u32_e64 s[54:55], v236, v204
	v_cndmask_b32_e64 v60, v67, v92, s[56:57]
	v_cmp_le_u32_e64 s[56:57], v238, v204
	v_cndmask_b32_e64 v61, v67, v93, s[58:59]
	v_cmp_le_u32_e64 s[58:59], v240, v204
	v_cndmask_b32_e64 v62, v67, v94, s[54:55]
	v_cmp_le_u32_e64 s[54:55], v242, v204
	v_cndmask_b32_e64 v63, v67, v95, s[56:57]
	v_cndmask_b32_e64 v64, v67, v96, s[58:59]
	v_cndmask_b32_e64 v65, v67, v97, s[54:55]
	v_mov_b32_e32 v34, v67
	v_mov_b32_e32 v35, v67
	v_mov_b32_e32 v36, v67
	v_mov_b32_e32 v37, v67
	v_mov_b32_e32 v38, v67
	v_mov_b32_e32 v39, v67
	v_mov_b32_e32 v40, v67
	v_mov_b32_e32 v41, v67
	v_mov_b32_e32 v42, v67
	v_mov_b32_e32 v43, v67
	v_mov_b32_e32 v44, v67
	v_mov_b32_e32 v45, v67
	v_mov_b32_e32 v46, v67
	v_mov_b32_e32 v47, v67
	v_mov_b32_e32 v48, v67
	v_mov_b32_e32 v49, v67
	v_max_f32_e32 v68, v50, v50
	v_add_f32_e32 v82, v203, v66
	s_mov_b32 s2, 0x41000000
	s_branch .Lpend_0f
.Lpodd_0f:
	s_nop 7
	s_nop 3
	v_mov_b32_e32 v67, 0xff800000
	v_or_b32_e32 v214, 0xe0, v210
	v_or_b32_e32 v213, 0xc0, v210
	v_or_b32_e32 v215, 0xe1, v210
	v_or_b32_e32 v216, 0xc2, v210
	v_or_b32_e32 v217, 0xe2, v210
	v_or_b32_e32 v218, 0xc3, v210
	v_or_b32_e32 v219, 0xe3, v210
	v_or_b32_e32 v220, 0xc8, v210
	v_or_b32_e32 v221, 0xe8, v210
	v_or_b32_e32 v222, 0xc9, v210
	v_or_b32_e32 v223, 0xe9, v210
	v_or_b32_e32 v224, 0xca, v210
	v_or_b32_e32 v225, 0xea, v210
	v_or_b32_e32 v226, 0xcb, v210
	v_or_b32_e32 v227, 0xeb, v210
	v_or_b32_e32 v228, 0xd0, v210
	v_or_b32_e32 v229, 0xf0, v210
	v_or_b32_e32 v230, 0xd1, v210
	v_or_b32_e32 v231, 0xf1, v210
	v_or_b32_e32 v232, 0xd2, v210
	v_or_b32_e32 v233, 0xf2, v210
	v_or_b32_e32 v234, 0xd3, v210
	v_or_b32_e32 v235, 0xf3, v210
	v_or_b32_e32 v236, 0xd8, v210
	v_or_b32_e32 v237, 0xf8, v210
	v_or_b32_e32 v238, 0xd9, v210
	v_or_b32_e32 v239, 0xf9, v210
	v_or_b32_e32 v240, 0xda, v210
	v_or_b32_e32 v241, 0xfa, v210
	v_or_b32_e32 v242, 0xdb, v210
	v_or_b32_e32 v243, 0xfb, v210
	v_cmp_le_u32_e64 s[54:55], v214, v204
	v_cmp_le_u32_e64 s[56:57], v215, v204
	v_cmp_le_u32_e64 s[58:59], v217, v204
	v_cndmask_b32_e64 v34, v67, v34, s[54:55]
	v_cmp_le_u32_e64 s[54:55], v219, v204
	v_cndmask_b32_e64 v35, v67, v35, s[56:57]
	v_cmp_le_u32_e64 s[56:57], v221, v204
	v_cndmask_b32_e64 v36, v67, v36, s[58:59]
	v_cmp_le_u32_e64 s[58:59], v223, v204
	v_cndmask_b32_e64 v37, v67, v37, s[54:55]
	v_cmp_le_u32_e64 s[54:55], v225, v204
	v_cndmask_b32_e64 v38, v67, v38, s[56:57]
	v_cmp_le_u32_e64 s[56:57], v227, v204
	v_cndmask_b32_e64 v39, v67, v39, s[58:59]
	v_cmp_le_u32_e64 s[58:59], v229, v204
	v_cndmask_b32_e64 v40, v67, v40, s[54:55]
	v_cmp_le_u32_e64 s[54:55], v231, v204
	v_cndmask_b32_e64 v41, v67, v41, s[56:57]
	v_cmp_le_u32_e64 s[56:57], v233, v204
	v_cndmask_b32_e64 v42, v67, v42, s[58:59]
	v_cmp_le_u32_e64 s[58:59], v235, v204
	v_cndmask_b32_e64 v43, v67, v43, s[54:55]
	v_cmp_le_u32_e64 s[54:55], v237, v204
	v_cndmask_b32_e64 v44, v67, v44, s[56:57]
	v_cmp_le_u32_e64 s[56:57], v239, v204
	v_cndmask_b32_e64 v45, v67, v45, s[58:59]
	v_cmp_le_u32_e64 s[58:59], v241, v204
	v_cndmask_b32_e64 v46, v67, v46, s[54:55]
	v_cmp_le_u32_e64 s[54:55], v243, v204
	v_cndmask_b32_e64 v47, v67, v47, s[56:57]
	v_cndmask_b32_e64 v48, v67, v48, s[58:59]
	v_cndmask_b32_e64 v49, v67, v49, s[54:55]
	v_mov_b32_e32 v51, v83
	v_mov_b32_e32 v50, v82
	v_mov_b32_e32 v52, v84
	v_mov_b32_e32 v53, v85
	v_mov_b32_e32 v54, v86
	v_mov_b32_e32 v55, v87
	v_mov_b32_e32 v56, v88
	v_mov_b32_e32 v57, v89
	v_mov_b32_e32 v58, v90
	v_mov_b32_e32 v59, v91
	v_mov_b32_e32 v60, v92
	v_mov_b32_e32 v61, v93
	v_mov_b32_e32 v62, v94
	v_mov_b32_e32 v63, v95
	v_mov_b32_e32 v64, v96
	v_mov_b32_e32 v65, v97
	v_max_f32_e32 v68, v50, v50
	v_add_f32_e32 v82, v203, v66
	s_mov_b32 s2, 0x41000000
.Lpend_0f:
.Lmend_0f:
	v_max_f32_e32 v67, v51, v51
	v_max_f32_e32 v67, v68, v67
	v_max3_f32 v68, v52, v53, v35
	v_max3_f32 v67, v67, v34, v36
	v_max3_f32 v67, v67, v37, v54
	v_max3_f32 v68, v68, v56, v57
	v_max3_f32 v67, v67, v55, v38
	v_max3_f32 v68, v68, v40, v41
	v_max3_f32 v67, v67, v39, v58
	v_max3_f32 v68, v68, v60, v61
	v_max3_f32 v67, v67, v59, v42
	v_max3_f32 v68, v68, v44, v45
	v_max3_f32 v67, v67, v43, v62
	v_max3_f32 v68, v68, v64, v65
	v_max3_f32 v67, v67, v63, v46
	v_max3_f32 v68, v68, v48, v49
	v_max3_f32 v66, v67, v47, v68
	v_mov_b32_e32 v67, v66
	s_nop 1
	v_permlane32_swap_b32_e32 v66, v67
	v_max_f32_e32 v67, v67, v67
	v_max_f32_e32 v66, v66, v66
	v_max_f32_e32 v66, v66, v67
	v_cmp_lt_f32_e32 vcc, s2, v66
	s_cmp_lg_u64 vcc, 0
	s_cselect_b64 s[2:3], -1, 0
	s_cbranch_vccnz .LBB1_160

.LBB1_80:
	v_add_f32_e32 v50, v50, v51
	v_add_f32_e32 v50, v52, v50
	v_add_f32_e32 v50, v53, v50
	v_add_f32_e32 v50, v54, v50
	v_add_f32_e32 v50, v55, v50
	v_add_f32_e32 v50, v56, v50
	v_add_f32_e32 v50, v57, v50
	v_add_f32_e32 v50, v58, v50
	v_add_f32_e32 v50, v59, v50
	v_add_f32_e32 v50, v60, v50
	v_add_f32_e32 v50, v61, v50
	v_add_f32_e32 v50, v62, v50
	v_add_f32_e32 v50, v63, v50
	v_add_f32_e32 v50, v64, v50
	v_add_f32_e32 v50, v65, v50
	v_add_f32_e32 v34, v34, v50
	v_add_f32_e32 v34, v35, v34
	v_add_f32_e32 v34, v36, v34
	v_add_f32_e32 v34, v37, v34
	v_add_f32_e32 v34, v38, v34
	v_add_f32_e32 v34, v39, v34
	v_add_f32_e32 v34, v40, v34
	v_add_f32_e32 v34, v41, v34
	v_add_f32_e32 v34, v42, v34
	v_add_f32_e32 v34, v43, v34
	v_add_f32_e32 v34, v44, v34
	v_add_f32_e32 v34, v45, v34
	v_add_f32_e32 v34, v46, v34
	v_add_f32_e32 v34, v47, v34
	v_add_f32_e32 v34, v48, v34
	v_add_f32_e32 v34, v49, v34
	v_add_f32_e32 v34, v82, v34
	v_mov_b32_e32 v35, v34
	s_nop 1
	v_permlane32_swap_b32_e32 v34, v35
	s_and_saveexec_b64 s[2:3], s[0:1]
	v_add_f32_e32 v34, v34, v35
	ds_write_b32 v198, v34 offset:49280
	s_or_b64 exec, exec, s[2:3]
	s_waitcnt lgkmcnt(0)
	ds_read_b128 v[34:37], v66 offset:49280
	ds_read_b128 v[38:41], v66 offset:49312
	s_mul_i32 s3, s35, 0xe80
	s_mul_hi_u32 s2, s35, 0xe80
	s_add_u32 s3, s10, s3
	s_waitcnt lgkmcnt(1)
	v_rcp_f32_e32 v42, v34
	v_rcp_f32_e32 v43, v35
	s_addc_u32 s4, s11, s2
	s_lshl_b32 s5, s34, 12
	v_lshlrev_b32_e32 v50, 1, v208
	v_lshlrev_b32_e32 v244, 9, v196
	v_rcp_f32_e32 v44, v36
	v_or3_b32 v50, s5, v50, v244
	v_fma_mixlo_f16 v2, v2, v42, 0
	ds_write_b16 v50, v2 offset:51200
	v_fma_mixlo_f16 v2, v18, v42, 0
	v_rcp_f32_e32 v45, v37
	ds_write_b16 v50, v2 offset:51264
	v_fma_mixlo_f16 v2, v3, v43, 0
	ds_write_b16 v50, v2 offset:51328
	v_fma_mixlo_f16 v2, v19, v43, 0
	s_waitcnt lgkmcnt(3)
	v_rcp_f32_e32 v46, v38
	ds_write_b16 v50, v2 offset:51392
	v_fma_mixlo_f16 v2, v4, v44, 0
	ds_write_b16 v50, v2 offset:51456
	v_fma_mixlo_f16 v2, v20, v44, 0
	v_rcp_f32_e32 v47, v39
	ds_write_b16 v50, v2 offset:51520
	v_fma_mixlo_f16 v2, v5, v45, 0
	ds_read_b128 v[34:37], v66 offset:49344
	ds_write_b16 v50, v2 offset:51584
	v_fma_mixlo_f16 v2, v21, v45, 0
	v_rcp_f32_e32 v48, v40
	ds_write_b16 v50, v2 offset:51648
	v_fma_mixlo_f16 v2, v6, v46, 0
	ds_write_b16 v50, v2 offset:52224
	v_fma_mixlo_f16 v2, v22, v46, 0
	v_rcp_f32_e32 v49, v41
	ds_write_b16 v50, v2 offset:52288
	v_fma_mixlo_f16 v2, v7, v47, 0
	ds_write_b16 v50, v2 offset:52352
	v_fma_mixlo_f16 v2, v23, v47, 0
	ds_read_b128 v[38:41], v66 offset:49376
	s_waitcnt lgkmcnt(6)
	v_rcp_f32_e32 v34, v34
	ds_write_b16 v50, v2 offset:52416
	v_fma_mixlo_f16 v2, v8, v48, 0
	ds_write_b16 v50, v2 offset:52480
	v_fma_mixlo_f16 v2, v24, v48, 0
	v_rcp_f32_e32 v35, v35
	ds_write_b16 v50, v2 offset:52544
	v_fma_mixlo_f16 v2, v9, v49, 0
	ds_write_b16 v50, v2 offset:52608
	v_fma_mixlo_f16 v2, v25, v49, 0
	v_rcp_f32_e32 v36, v36
	ds_write_b16 v50, v2 offset:52672
	v_fma_mixlo_f16 v2, v10, v34, 0
	ds_write_b16 v50, v2 offset:53248
	v_fma_mixlo_f16 v2, v26, v34, 0
	v_rcp_f32_e32 v37, v37
	ds_write_b16 v50, v2 offset:53312
	v_fma_mixlo_f16 v2, v11, v35, 0
	ds_write_b16 v50, v2 offset:53376
	v_fma_mixlo_f16 v2, v27, v35, 0
	s_waitcnt lgkmcnt(8)
	v_rcp_f32_e32 v38, v38
	ds_write_b16 v50, v2 offset:53440
	v_fma_mixlo_f16 v2, v12, v36, 0
	ds_write_b16 v50, v2 offset:53504
	v_fma_mixlo_f16 v2, v28, v36, 0
	v_rcp_f32_e32 v39, v39
	ds_write_b16 v50, v2 offset:53568
	v_fma_mixlo_f16 v2, v13, v37, 0
	ds_write_b16 v50, v2 offset:53632
	v_fma_mixlo_f16 v2, v29, v37, 0
	v_rcp_f32_e32 v40, v40
	ds_write_b16 v50, v2 offset:53696
	v_fma_mixlo_f16 v2, v14, v38, 0
	ds_write_b16 v50, v2 offset:54272
	v_fma_mixlo_f16 v2, v30, v38, 0
	v_rcp_f32_e32 v41, v41
	ds_write_b16 v50, v2 offset:54336
	v_fma_mixlo_f16 v2, v15, v39, 0
	ds_write_b16 v50, v2 offset:54400
	v_fma_mixlo_f16 v2, v31, v39, 0
	ds_write_b16 v50, v2 offset:54464
	v_fma_mixlo_f16 v2, v16, v40, 0
	ds_write_b16 v50, v2 offset:54528
	v_fma_mixlo_f16 v2, v32, v40, 0
	ds_write_b16 v50, v2 offset:54592
	v_fma_mixlo_f16 v2, v17, v41, 0
	ds_write_b16 v50, v2 offset:54656
	v_fma_mixlo_f16 v2, v33, v41, 0
	ds_write_b16 v50, v2 offset:54720
	v_and_b32_e32 v2, 56, v197
	v_lshrrev_b32_e32 v8, 3, v195
	v_lshlrev_b32_e32 v204, 1, v2
	s_add_u32 s2, s3, s14
	v_or_b32_e32 v14, s5, v204
	v_lshlrev_b32_e32 v245, 7, v8
	s_addc_u32 s3, s4, s15
	s_waitcnt lgkmcnt(0)
	v_mov_b32_e32 v205, 0
	v_or_b32_e32 v2, v14, v245
	v_mul_u32_u24_e32 v8, 0x740, v8
	v_lshl_add_u64 v[6:7], s[2:3], 0, v[204:205]
	ds_read_b128 v[2:5], v2 offset:51200
	v_lshlrev_b32_e32 v206, 1, v8
	v_mov_b32_e32 v207, v205
	v_or_b32_e32 v246, 0x400, v245
	v_lshl_add_u64 v[10:11], v[6:7], 0, v[206:207]
	v_or_b32_e32 v6, v14, v246
	ds_read_b128 v[6:9], v6 offset:51200
	s_movk_i32 s2, 0x7000
	s_waitcnt lgkmcnt(1)
	global_store_dwordx4 v[10:11], v[2:5], off sc0 sc1
	v_or_b32_e32 v247, 0x800, v245
	v_or_b32_e32 v248, 0xc00, v245
	v_add_co_u32_e32 v2, vcc, s2, v10
	s_mov_b32 s2, 0xe000
	s_nop 0
	v_addc_co_u32_e32 v3, vcc, 0, v11, vcc
	s_waitcnt lgkmcnt(0)
	global_store_dwordx4 v[2:3], v[6:9], off offset:1024 sc0 sc1
	v_or_b32_e32 v2, v14, v247
	ds_read_b128 v[2:5], v2 offset:51200
	v_or_b32_e32 v6, v14, v248
	ds_read_b128 v[6:9], v6 offset:51200
	v_add_co_u32_e32 v12, vcc, s2, v10
	s_nop 1
	v_addc_co_u32_e32 v13, vcc, 0, v11, vcc
	s_waitcnt lgkmcnt(1)
	global_store_dwordx4 v[12:13], v[2:5], off offset:2048 sc0 sc1
	s_nop 1
	v_add_co_u32_e32 v2, vcc, 0x15000, v10
	s_nop 1
	v_addc_co_u32_e32 v3, vcc, 0, v11, vcc
	s_waitcnt lgkmcnt(0)
	global_store_dwordx4 v[2:3], v[6:9], off offset:3072 sc0 sc1
	s_waitcnt lgkmcnt(0)
	s_barrier
	s_andn2_b64 vcc, exec, s[12:13]
	s_cbranch_vccnz .LBB1_109
	s_mov_b32 s2, 0x14800
	v_mov_b32_e32 v2, v205
	v_mov_b32_e32 v3, v205
	v_mov_b32_e32 v4, v205
	v_mov_b32_e32 v5, v205
	v_mov_b32_e32 v6, v205
	v_mov_b32_e32 v7, v205
	v_mov_b32_e32 v8, v205
	v_mov_b32_e32 v9, v205
	v_mov_b32_e32 v10, v205
	v_mov_b32_e32 v11, v205
	v_mov_b32_e32 v12, v205
	v_mov_b32_e32 v13, v205
	v_mov_b32_e32 v14, v205
	v_mov_b32_e32 v15, v205
	v_mov_b32_e32 v16, v205
	v_mov_b32_e32 v17, v205
	v_add3_u32 v250, v194, v193, s2
	s_waitcnt vmcnt(4) lgkmcnt(0)
	s_barrier
	ds_read_b128 v[34:37], v250
	s_waitcnt lgkmcnt(0)
	v_mfma_f32_32x32x16_f16 v[18:33], v[34:37], v[140:143], v[2:17]
	ds_read_b128 v[34:37], v250 offset:512
	v_readfirstlane_b32 s4, v0
	s_lshr_b32 s18, s4, 6
	s_lshl_b32 s19, s18, 5
	s_cmp_lg_u32 s30, 0
	s_cselect_b64 s[2:3], -1, 0
	v_or_b32_e32 v207, s19, v208
	s_waitcnt lgkmcnt(0)
	v_mfma_f32_32x32x16_f16 v[2:17], v[34:37], v[140:143], v[2:17]
	ds_read_b128 v[34:37], v250 offset:2048
	s_and_b64 vcc, exec, s[2:3]
	s_waitcnt lgkmcnt(0)
	v_mfma_f32_32x32x16_f16 v[18:33], v[34:37], v[136:139], v[18:33]
	ds_read_b128 v[34:37], v250 offset:2560
	s_waitcnt lgkmcnt(0)
	v_mfma_f32_32x32x16_f16 v[2:17], v[34:37], v[136:139], v[2:17]
	ds_read_b128 v[34:37], v250 offset:4096
	s_waitcnt lgkmcnt(0)
	v_mfma_f32_32x32x16_f16 v[18:33], v[34:37], v[132:135], v[18:33]
	ds_read_b128 v[34:37], v250 offset:4608
	s_waitcnt lgkmcnt(0)
	v_mfma_f32_32x32x16_f16 v[2:17], v[34:37], v[132:135], v[2:17]
	ds_read_b128 v[34:37], v250 offset:6144
	s_waitcnt lgkmcnt(0)
	v_mfma_f32_32x32x16_f16 v[18:33], v[34:37], v[128:131], v[18:33]
	ds_read_b128 v[34:37], v250 offset:6656
	s_waitcnt lgkmcnt(0)
	v_mfma_f32_32x32x16_f16 v[2:17], v[34:37], v[128:131], v[2:17]
	s_nop 15
	s_nop 7
	s_cbranch_vccnz .LBB1_85
	s_cmp_lg_u32 s50, 0
	s_cbranch_scc1 .LBB1_85
	s_cmp_lg_u32 s52, 0
	s_cbranch_scc1 .Lpodd_pr
	s_nop 7
	s_nop 3
	v_mov_b32_e32 v34, 0xff800000
	v_cmp_lt_u32_e64 s[54:55], v210, v207
	v_cmp_le_u32_e64 s[56:57], v210, v207
	v_or_b32_e32 v0, 2, v210
	v_cmp_le_u32_e64 s[58:59], v0, v207
	v_cndmask_b32_e64 v19, v34, v19, s[54:55]
	v_or_b32_e32 v0, 3, v210
	v_cmp_le_u32_e64 s[54:55], v0, v207
	v_cndmask_b32_e64 v18, v34, v18, s[56:57]
	v_or_b32_e32 v0, 8, v210
	v_cmp_le_u32_e64 s[56:57], v0, v207
	v_cndmask_b32_e64 v20, v34, v20, s[58:59]
	v_or_b32_e32 v0, 9, v210
	v_cmp_le_u32_e64 s[58:59], v0, v207
	v_cndmask_b32_e64 v21, v34, v21, s[54:55]
	v_or_b32_e32 v0, 10, v210
	v_cmp_le_u32_e64 s[54:55], v0, v207
	v_cndmask_b32_e64 v22, v34, v22, s[56:57]
	v_or_b32_e32 v0, 11, v210
	v_cmp_le_u32_e64 s[56:57], v0, v207
	v_cndmask_b32_e64 v23, v34, v23, s[58:59]
	v_or_b32_e32 v0, 16, v210
	v_cmp_le_u32_e64 s[58:59], v0, v207
	v_cndmask_b32_e64 v24, v34, v24, s[54:55]
	v_or_b32_e32 v0, 17, v210
	v_cmp_le_u32_e64 s[54:55], v0, v207
	v_cndmask_b32_e64 v25, v34, v25, s[56:57]
	v_or_b32_e32 v0, 18, v210
	v_cmp_le_u32_e64 s[56:57], v0, v207
	v_cndmask_b32_e64 v26, v34, v26, s[58:59]
	v_or_b32_e32 v0, 19, v210
	v_cmp_le_u32_e64 s[58:59], v0, v207
	v_cndmask_b32_e64 v27, v34, v27, s[54:55]
	v_or_b32_e32 v0, 24, v210
	v_cmp_le_u32_e64 s[54:55], v0, v207
	v_cndmask_b32_e64 v28, v34, v28, s[56:57]
	v_or_b32_e32 v0, 25, v210
	v_cmp_le_u32_e64 s[56:57], v0, v207
	v_cndmask_b32_e64 v29, v34, v29, s[58:59]
	v_or_b32_e32 v0, 26, v210
	v_cmp_le_u32_e64 s[58:59], v0, v207
	v_cndmask_b32_e64 v30, v34, v30, s[54:55]
	v_or_b32_e32 v0, 27, v210
	v_cmp_le_u32_e64 s[54:55], v0, v207
	v_cndmask_b32_e64 v31, v34, v31, s[56:57]
	v_cndmask_b32_e64 v32, v34, v32, s[58:59]
	v_cndmask_b32_e64 v33, v34, v33, s[54:55]
	v_mov_b32_e32 v2, v34
	v_mov_b32_e32 v3, v34
	v_mov_b32_e32 v4, v34
	v_mov_b32_e32 v5, v34
	v_mov_b32_e32 v6, v34
	v_mov_b32_e32 v7, v34
	v_mov_b32_e32 v8, v34
	v_mov_b32_e32 v9, v34
	v_mov_b32_e32 v10, v34
	v_mov_b32_e32 v11, v34
	v_mov_b32_e32 v12, v34
	v_mov_b32_e32 v13, v34
	v_mov_b32_e32 v14, v34
	v_mov_b32_e32 v15, v34
	v_mov_b32_e32 v16, v34
	v_mov_b32_e32 v17, v34
	s_branch .Lpend_pr
.Lpodd_pr:
	s_nop 7
	s_nop 3
	v_mov_b32_e32 v34, 0xff800000
	v_or_b32_e32 v0, 32, v210
	v_cmp_le_u32_e64 s[54:55], v0, v207
	v_or_b32_e32 v0, 33, v210
	v_cmp_le_u32_e64 s[56:57], v0, v207
	v_or_b32_e32 v0, 34, v210
	v_cmp_le_u32_e64 s[58:59], v0, v207
	v_cndmask_b32_e64 v2, v34, v2, s[54:55]
	v_or_b32_e32 v0, 35, v210
	v_cmp_le_u32_e64 s[54:55], v0, v207
	v_cndmask_b32_e64 v3, v34, v3, s[56:57]
	v_or_b32_e32 v0, 40, v210
	v_cmp_le_u32_e64 s[56:57], v0, v207
	v_cndmask_b32_e64 v4, v34, v4, s[58:59]
	v_or_b32_e32 v0, 41, v210
	v_cmp_le_u32_e64 s[58:59], v0, v207
	v_cndmask_b32_e64 v5, v34, v5, s[54:55]
	v_or_b32_e32 v0, 42, v210
	v_cmp_le_u32_e64 s[54:55], v0, v207
	v_cndmask_b32_e64 v6, v34, v6, s[56:57]
	v_or_b32_e32 v0, 43, v210
	v_cmp_le_u32_e64 s[56:57], v0, v207
	v_cndmask_b32_e64 v7, v34, v7, s[58:59]
	v_or_b32_e32 v0, 48, v210
	v_cmp_le_u32_e64 s[58:59], v0, v207
	v_cndmask_b32_e64 v8, v34, v8, s[54:55]
	v_or_b32_e32 v0, 49, v210
	v_cmp_le_u32_e64 s[54:55], v0, v207
	v_cndmask_b32_e64 v9, v34, v9, s[56:57]
	v_or_b32_e32 v0, 50, v210
	v_cmp_le_u32_e64 s[56:57], v0, v207
	v_cndmask_b32_e64 v10, v34, v10, s[58:59]
	v_or_b32_e32 v0, 51, v210
	v_cmp_le_u32_e64 s[58:59], v0, v207
	v_cndmask_b32_e64 v11, v34, v11, s[54:55]
	v_or_b32_e32 v0, 56, v210
	v_cmp_le_u32_e64 s[54:55], v0, v207
	v_cndmask_b32_e64 v12, v34, v12, s[56:57]
	v_or_b32_e32 v0, 57, v210
	v_cmp_le_u32_e64 s[56:57], v0, v207
	v_cndmask_b32_e64 v13, v34, v13, s[58:59]
	v_or_b32_e32 v0, 58, v210
	v_cmp_le_u32_e64 s[58:59], v0, v207
	v_cndmask_b32_e64 v14, v34, v14, s[54:55]
	v_or_b32_e32 v0, 59, v210
	v_cmp_le_u32_e64 s[54:55], v0, v207
	v_cndmask_b32_e64 v15, v34, v15, s[56:57]
	v_cndmask_b32_e64 v16, v34, v16, s[58:59]
	v_cndmask_b32_e64 v17, v34, v17, s[54:55]
.Lpend_pr:
.LBB1_85:
	s_add_i32 s33, s33, s28
	s_lshr_b32 s5, s33, 31
	s_ashr_i32 s12, s33, 2
	s_add_i32 s5, s12, s5
	s_add_i32 s12, s5, s31
	s_ashr_i32 s13, s12, 31
	v_add3_u32 v0, v191, v1, v192
	s_lshl_b32 s20, s30, 8
	s_lshl_b64 s[12:13], s[12:13], 18
	v_or_b32_e32 v251, 0x1a800, v0
	v_max3_f32 v0, v18, v19, v2
	s_add_u32 s5, s6, s12
	v_max3_f32 v1, v20, v21, v3
	v_max3_f32 v0, v0, v4, v5
	s_addc_u32 s6, s7, s13
	v_max3_f32 v0, v0, v22, v23
	v_max3_f32 v1, v1, v24, v25
	s_add_u32 s7, s8, s12
	v_max3_f32 v0, v0, v6, v7
	v_max3_f32 v1, v1, v8, v9
	s_addc_u32 s8, s9, s13
	s_and_b32 s4, s4, 0x3fffffc0
	v_max3_f32 v0, v0, v26, v27
	v_max3_f32 v1, v1, v28, v29
	s_lshl_b32 s21, s4, 2
	s_lshl_b32 s23, s18, 10
	v_max3_f32 v0, v0, v10, v11
	v_max3_f32 v1, v1, v12, v13
	s_add_u32 s13, s5, s23
	v_max3_f32 v0, v0, v30, v31
	v_max3_f32 v1, v1, v32, v33
	s_addc_u32 s14, s6, 0
	v_max3_f32 v0, v0, v14, v15
	v_max3_f32 v1, v1, v16, v17
	s_add_u32 s15, s7, s23
	v_max_f32_e32 v0, v0, v1
	s_addc_u32 s16, s8, 0
	v_mov_b32_e32 v1, v0
	s_add_i32 s4, s20, 0x100
	s_nop 0
	v_permlane32_swap_b32_e32 v0, v1
	s_add_i32 s22, s23, 0x14800
	s_add_i32 s23, s23, 0x1a800
	s_lshr_b32 s24, s4, 6
	v_max_f32_e32 v0, v0, v1
	v_mov_b32_e32 v64, 0
	v_add_f32_e32 v249, v64, v0
	v_sub_f32_e32 v1, v18, v0
	v_sub_f32_e32 v18, v19, v0
	v_sub_f32_e32 v19, v20, v0
	v_sub_f32_e32 v20, v21, v0
	v_sub_f32_e32 v21, v22, v0
	v_sub_f32_e32 v22, v23, v0
	v_sub_f32_e32 v23, v24, v0
	v_sub_f32_e32 v24, v25, v0
	v_sub_f32_e32 v25, v26, v0
	v_sub_f32_e32 v26, v27, v0
	v_sub_f32_e32 v27, v28, v0
	v_sub_f32_e32 v28, v29, v0
	v_sub_f32_e32 v29, v30, v0
	v_sub_f32_e32 v30, v31, v0
	v_sub_f32_e32 v31, v32, v0
	s_nop 0
	v_xor_b32_e32 v32, 0x80000000, v249
	v_sub_f32_e32 v48, v33, v0
	v_mov_b32_e32 v33, v32
	v_mov_b32_e32 v34, v32
	v_mov_b32_e32 v35, v32
	v_mov_b32_e32 v36, v32
	v_mov_b32_e32 v37, v32
	v_mov_b32_e32 v38, v32
	v_mov_b32_e32 v39, v32
	v_mov_b32_e32 v40, v32
	v_mov_b32_e32 v41, v32
	v_mov_b32_e32 v42, v32
	v_mov_b32_e32 v43, v32
	v_mov_b32_e32 v44, v32
	v_mov_b32_e32 v45, v32
	v_mov_b32_e32 v46, v32
	v_mov_b32_e32 v47, v32
	s_add_u32 s4, s13, 0x6000
	s_waitcnt vmcnt(0) lgkmcnt(0)
	s_barrier
	s_addc_u32 s5, s14, 0
	s_mov_b32 s6, m0
	s_mov_b32 m0, s22
	s_nop 0
	global_load_lds_dwordx4 v211, s[4:5]
	s_mov_b32 m0, s6
	s_add_u32 s4, s15, 0x2000
	s_addc_u32 s5, s16, 0
	s_add_i32 s6, s23, 0x2000
	s_mov_b32 s7, m0
	s_mov_b32 m0, s6
	s_nop 0
	global_load_lds_dwordx4 v211, s[4:5]
	s_mov_b32 m0, s7
	ds_read_b128 v[188:191], v250 offset:8192
	ds_read_b128 v[184:187], v250 offset:8704
	ds_read_b128 v[180:183], v250 offset:10240
	ds_read_b128 v[176:179], v250 offset:10752
	ds_read_b128 v[172:175], v250 offset:12288
	ds_read_b128 v[168:171], v250 offset:12800
	ds_read_b128 v[164:167], v250 offset:14336
	ds_read_b128 v[160:163], v250 offset:14848
	v_sub_f32_e32 v2, v2, v0
	v_sub_f32_e32 v3, v3, v0
	v_sub_f32_e32 v4, v4, v0
	v_sub_f32_e32 v5, v5, v0
	v_sub_f32_e32 v6, v6, v0
	v_sub_f32_e32 v7, v7, v0
	v_sub_f32_e32 v8, v8, v0
	v_sub_f32_e32 v9, v9, v0
	v_sub_f32_e32 v10, v10, v0
	v_sub_f32_e32 v11, v11, v0
	v_sub_f32_e32 v12, v12, v0
	v_sub_f32_e32 v13, v13, v0
	v_sub_f32_e32 v14, v14, v0
	v_sub_f32_e32 v15, v15, v0
	v_sub_f32_e32 v16, v16, v0
	v_sub_f32_e32 v0, v17, v0
	v_exp_f32_e32 v80, v1
	v_exp_f32_e32 v81, v18
	v_exp_f32_e32 v82, v19
	v_exp_f32_e32 v83, v20
	v_exp_f32_e32 v84, v21
	v_exp_f32_e32 v85, v22
	v_exp_f32_e32 v86, v23
	v_exp_f32_e32 v87, v24
	v_exp_f32_e32 v88, v25
	v_exp_f32_e32 v89, v26
	v_exp_f32_e32 v90, v27
	v_exp_f32_e32 v91, v28
	v_exp_f32_e32 v92, v29
	v_exp_f32_e32 v93, v30
	v_exp_f32_e32 v94, v31
	v_exp_f32_e32 v95, v48
	v_exp_f32_e32 v48, v2
	v_exp_f32_e32 v49, v3
	v_exp_f32_e32 v50, v4
	v_exp_f32_e32 v51, v5
	v_exp_f32_e32 v52, v6
	v_exp_f32_e32 v53, v7
	v_exp_f32_e32 v54, v8
	v_exp_f32_e32 v55, v9
	v_exp_f32_e32 v56, v10
	v_exp_f32_e32 v57, v11
	v_exp_f32_e32 v58, v12
	v_exp_f32_e32 v59, v13
	v_exp_f32_e32 v60, v14
	v_exp_f32_e32 v61, v15
	v_exp_f32_e32 v62, v16
	v_exp_f32_e32 v63, v0
	s_waitcnt vmcnt(2) lgkmcnt(0)
	s_barrier
	s_mov_b32 s12, 0
	s_movk_i32 s25, 0x2000
	s_mov_b32 s6, 0
	s_mov_b32 s4, 1
	s_andn2_b64 vcc, exec, s[2:3]
	v_lshl_add_u32 v205, v208, 2, s21
	s_cbranch_vccnz .LBB1_101
	s_add_u32 s2, s15, 0x6000
	v_mov_b32_e32 v0, 0
	s_addc_u32 s3, s16, 0
	v_mov_b32_e32 v14, v0
	v_mov_b32_e32 v15, v0
	s_add_u32 s4, s13, 0xa000
	v_mov_b32_e32 v1, v0
	v_mov_b32_e32 v2, v0
	v_mov_b32_e32 v3, v0
	v_mov_b32_e32 v4, v0
	v_mov_b32_e32 v5, v0
	v_mov_b32_e32 v6, v0
	v_mov_b32_e32 v7, v0
	v_mov_b32_e32 v8, v0
	v_mov_b32_e32 v9, v0
	v_mov_b32_e32 v10, v0
	v_mov_b32_e32 v11, v0
	v_mov_b32_e32 v12, v0
	v_mov_b32_e32 v13, v0
	v_mov_b64_e32 v[30:31], v[14:15]
	s_addc_u32 s5, s14, 0
	s_movk_i32 s12, 0x4000
	s_movk_i32 s30, 0x2000
	s_mov_b32 s27, 6
	s_mov_b32 s17, 0x41000000
	v_mov_b64_e32 v[28:29], v[12:13]
	v_mov_b64_e32 v[26:27], v[10:11]
	v_mov_b64_e32 v[24:25], v[8:9]
	v_mov_b64_e32 v[22:23], v[6:7]
	v_mov_b64_e32 v[20:21], v[4:5]
	v_mov_b64_e32 v[18:19], v[2:3]
	v_mov_b64_e32 v[16:17], v[0:1]
	v_mov_b32_e32 v64, v0

.LBB1_103:
	v_add_u32_e32 v65, s26, v251
	ds_read_b64_tr_b16 v[124:125], v65
	ds_read_b64_tr_b16 v[126:127], v65 offset:512
	s_waitcnt lgkmcnt(9)
	v_mfma_f32_32x32x16_f16 v[96:111], v[188:191], v[140:143], v[32:47]
	v_add_f32_e32 v66, v80, v81
	v_add_f32_e32 v66, v82, v66
	v_add_f32_e32 v66, v83, v66
	v_add_f32_e32 v66, v84, v66
	v_add_f32_e32 v66, v85, v66
	v_cvt_pk_f16_f32 v156, v80, v81
	v_cvt_pk_f16_f32 v157, v82, v83
	ds_read_b64_tr_b16 v[120:121], v65 offset:4096
	ds_read_b64_tr_b16 v[122:123], v65 offset:4608
	s_waitcnt lgkmcnt(10)
	v_mfma_f32_32x32x16_f16 v[32:47], v[184:187], v[140:143], v[32:47]
	v_add_f32_e32 v66, v86, v66
	v_add_f32_e32 v66, v87, v66
	v_add_f32_e32 v66, v88, v66
	v_add_f32_e32 v66, v89, v66
	v_cvt_pk_f16_f32 v158, v84, v85
	v_cvt_pk_f16_f32 v159, v86, v87
	ds_read_b64_tr_b16 v[116:117], v65 offset:1024
	ds_read_b64_tr_b16 v[118:119], v65 offset:1536
	s_waitcnt lgkmcnt(11)
	v_mfma_f32_32x32x16_f16 v[96:111], v[180:183], v[136:139], v[96:111]
	v_add_f32_e32 v66, v90, v66
	v_add_f32_e32 v66, v91, v66
	v_add_f32_e32 v66, v92, v66
	v_add_f32_e32 v66, v93, v66
	v_cvt_pk_f16_f32 v152, v88, v89
	v_cvt_pk_f16_f32 v153, v90, v91
	ds_read_b64_tr_b16 v[112:113], v65 offset:5120
	ds_read_b64_tr_b16 v[114:115], v65 offset:5632
	s_waitcnt lgkmcnt(12)
	v_mfma_f32_32x32x16_f16 v[32:47], v[176:179], v[136:139], v[32:47]
	v_add_f32_e32 v66, v94, v66
	v_add_f32_e32 v66, v95, v66
	v_add_f32_e32 v66, v48, v66
	v_add_f32_e32 v66, v49, v66
	v_cvt_pk_f16_f32 v154, v92, v93
	v_cvt_pk_f16_f32 v155, v94, v95
	ds_read_b64_tr_b16 v[92:93], v65 offset:2048
	ds_read_b64_tr_b16 v[94:95], v65 offset:2560
	s_waitcnt lgkmcnt(13)
	v_mfma_f32_32x32x16_f16 v[96:111], v[172:175], v[132:135], v[96:111]
	v_add_f32_e32 v66, v50, v66
	v_add_f32_e32 v66, v51, v66
	v_add_f32_e32 v66, v52, v66
	v_add_f32_e32 v66, v53, v66
	v_cvt_pk_f16_f32 v148, v48, v49
	v_cvt_pk_f16_f32 v149, v50, v51
	ds_read_b64_tr_b16 v[88:89], v65 offset:6144
	ds_read_b64_tr_b16 v[90:91], v65 offset:6656
	s_waitcnt lgkmcnt(14)
	v_mfma_f32_32x32x16_f16 v[32:47], v[168:171], v[132:135], v[32:47]
	v_add_f32_e32 v48, v54, v66
	v_add_f32_e32 v48, v55, v48
	v_add_f32_e32 v48, v56, v48
	v_add_f32_e32 v48, v57, v48
	v_cvt_pk_f16_f32 v150, v52, v53
	v_cvt_pk_f16_f32 v151, v54, v55
	ds_read_b64_tr_b16 v[84:85], v65 offset:3072
	ds_read_b64_tr_b16 v[86:87], v65 offset:3584
	s_waitcnt lgkmcnt(14)
	v_mfma_f32_32x32x16_f16 v[96:111], v[164:167], v[128:131], v[96:111]
	v_add_f32_e32 v48, v58, v48
	v_add_f32_e32 v48, v59, v48
	v_add_f32_e32 v48, v60, v48
	v_add_f32_e32 v48, v61, v48
	v_cvt_pk_f16_f32 v144, v56, v57
	v_cvt_pk_f16_f32 v145, v58, v59
	ds_read_b64_tr_b16 v[80:81], v65 offset:7168
	ds_read_b64_tr_b16 v[82:83], v65 offset:7680
	v_mfma_f32_32x32x16_f16 v[32:47], v[160:163], v[128:131], v[32:47]
	v_add_f32_e32 v48, v62, v48
	v_add_f32_e32 v48, v63, v48
	v_add_f32_e32 v65, 0, v48
	v_cvt_pk_f16_f32 v146, v60, v61
	v_cvt_pk_f16_f32 v147, v62, v63
	s_cmp_lt_u32 s50, 3
	s_cbranch_scc1 .Lmfill_1f
	s_cmp_lg_u32 s52, 0
	s_cbranch_scc1 .Lpodd_1f
	s_nop 7
	s_nop 3
	v_mov_b32_e32 v66, 0xff800000
	v_cmp_lt_u32_e64 s[54:55], v213, v207
	v_cmp_le_u32_e64 s[56:57], v213, v207
	v_cmp_le_u32_e64 s[58:59], v216, v207
	v_cndmask_b32_e64 v49, v66, v97, s[54:55]
	v_cmp_le_u32_e64 s[54:55], v218, v207
	v_cndmask_b32_e64 v48, v66, v96, s[56:57]
	v_cmp_le_u32_e64 s[56:57], v220, v207
	v_cndmask_b32_e64 v50, v66, v98, s[58:59]
	v_cmp_le_u32_e64 s[58:59], v222, v207
	v_cndmask_b32_e64 v51, v66, v99, s[54:55]
	v_cmp_le_u32_e64 s[54:55], v224, v207
	v_cndmask_b32_e64 v52, v66, v100, s[56:57]
	v_cmp_le_u32_e64 s[56:57], v226, v207
	v_cndmask_b32_e64 v53, v66, v101, s[58:59]
	v_cmp_le_u32_e64 s[58:59], v228, v207
	v_cndmask_b32_e64 v54, v66, v102, s[54:55]
	v_cmp_le_u32_e64 s[54:55], v230, v207
	v_cndmask_b32_e64 v55, v66, v103, s[56:57]
	v_cmp_le_u32_e64 s[56:57], v232, v207
	v_cndmask_b32_e64 v56, v66, v104, s[58:59]
	v_cmp_le_u32_e64 s[58:59], v234, v207
	v_cndmask_b32_e64 v57, v66, v105, s[54:55]
	v_cmp_le_u32_e64 s[54:55], v236, v207
	v_cndmask_b32_e64 v58, v66, v106, s[56:57]
	v_cmp_le_u32_e64 s[56:57], v238, v207
	v_cndmask_b32_e64 v59, v66, v107, s[58:59]
	v_cmp_le_u32_e64 s[58:59], v240, v207
	v_cndmask_b32_e64 v60, v66, v108, s[54:55]
	v_cmp_le_u32_e64 s[54:55], v242, v207
	v_cndmask_b32_e64 v61, v66, v109, s[56:57]
	v_cndmask_b32_e64 v62, v66, v110, s[58:59]
	v_cndmask_b32_e64 v63, v66, v111, s[54:55]
	v_mov_b32_e32 v32, v66
	v_mov_b32_e32 v33, v66
	v_mov_b32_e32 v34, v66
	v_mov_b32_e32 v35, v66
	v_mov_b32_e32 v36, v66
	v_mov_b32_e32 v37, v66
	v_mov_b32_e32 v38, v66
	v_mov_b32_e32 v39, v66
	v_mov_b32_e32 v40, v66
	v_mov_b32_e32 v41, v66
	v_mov_b32_e32 v42, v66
	v_mov_b32_e32 v43, v66
	v_mov_b32_e32 v44, v66
	v_mov_b32_e32 v45, v66
	v_mov_b32_e32 v46, v66
	v_mov_b32_e32 v47, v66
	s_mov_b32 s2, 0x41000000
	v_max_f32_e32 v67, v48, v48
	v_add_f32_e32 v96, v64, v65
	s_branch .Lpend_1f
.Lpodd_1f:
	s_nop 7
	s_nop 3
	v_mov_b32_e32 v66, 0xff800000
	v_cmp_le_u32_e64 s[54:55], v214, v207
	v_cmp_le_u32_e64 s[56:57], v215, v207
	v_cmp_le_u32_e64 s[58:59], v217, v207
	v_cndmask_b32_e64 v32, v66, v32, s[54:55]
	v_cmp_le_u32_e64 s[54:55], v219, v207
	v_cndmask_b32_e64 v33, v66, v33, s[56:57]
	v_cmp_le_u32_e64 s[56:57], v221, v207
	v_cndmask_b32_e64 v34, v66, v34, s[58:59]
	v_cmp_le_u32_e64 s[58:59], v223, v207
	v_cndmask_b32_e64 v35, v66, v35, s[54:55]
	v_cmp_le_u32_e64 s[54:55], v225, v207
	v_cndmask_b32_e64 v36, v66, v36, s[56:57]
	v_cmp_le_u32_e64 s[56:57], v227, v207
	v_cndmask_b32_e64 v37, v66, v37, s[58:59]
	v_cmp_le_u32_e64 s[58:59], v229, v207
	v_cndmask_b32_e64 v38, v66, v38, s[54:55]
	v_cmp_le_u32_e64 s[54:55], v231, v207
	v_cndmask_b32_e64 v39, v66, v39, s[56:57]
	v_cmp_le_u32_e64 s[56:57], v233, v207
	v_cndmask_b32_e64 v40, v66, v40, s[58:59]
	v_cmp_le_u32_e64 s[58:59], v235, v207
	v_cndmask_b32_e64 v41, v66, v41, s[54:55]
	v_cmp_le_u32_e64 s[54:55], v237, v207
	v_cndmask_b32_e64 v42, v66, v42, s[56:57]
	v_cmp_le_u32_e64 s[56:57], v239, v207
	v_cndmask_b32_e64 v43, v66, v43, s[58:59]
	v_cmp_le_u32_e64 s[58:59], v241, v207
	v_cndmask_b32_e64 v44, v66, v44, s[54:55]
	v_cmp_le_u32_e64 s[54:55], v243, v207
	v_cndmask_b32_e64 v45, v66, v45, s[56:57]
	v_cndmask_b32_e64 v46, v66, v46, s[58:59]
	v_cndmask_b32_e64 v47, v66, v47, s[54:55]
	v_mov_b32_e32 v49, v97
	v_mov_b32_e32 v48, v96
	v_mov_b32_e32 v50, v98
	v_mov_b32_e32 v51, v99
	v_mov_b32_e32 v52, v100
	v_mov_b32_e32 v53, v101
	v_mov_b32_e32 v54, v102
	v_mov_b32_e32 v55, v103
	v_mov_b32_e32 v56, v104
	v_mov_b32_e32 v57, v105
	v_mov_b32_e32 v58, v106
	v_mov_b32_e32 v59, v107
	v_mov_b32_e32 v60, v108
	v_mov_b32_e32 v61, v109
	v_mov_b32_e32 v62, v110
	v_mov_b32_e32 v63, v111
	s_mov_b32 s2, 0x41000000
	v_max_f32_e32 v67, v48, v48
	v_add_f32_e32 v96, v64, v65
.Lpend_1f:
.Lmend_1f:
	v_max_f32_e32 v66, v49, v49
	v_max_f32_e32 v66, v67, v66
	v_max3_f32 v67, v50, v51, v33
	v_max3_f32 v66, v66, v32, v34
	v_max3_f32 v66, v66, v35, v52
	v_max3_f32 v67, v67, v54, v55
	v_max3_f32 v66, v66, v53, v36
	v_max3_f32 v67, v67, v38, v39
	v_max3_f32 v66, v66, v37, v56
	v_max3_f32 v67, v67, v58, v59
	v_max3_f32 v66, v66, v57, v40
	v_max3_f32 v67, v67, v42, v43
	v_max3_f32 v66, v66, v41, v60
	v_max3_f32 v67, v67, v62, v63
	v_max3_f32 v66, v66, v61, v44
	v_max3_f32 v67, v67, v46, v47
	v_max3_f32 v64, v66, v45, v67
	v_mov_b32_e32 v65, v64
	s_nop 1
	v_permlane32_swap_b32_e32 v64, v65
	v_max_f32_e32 v65, v65, v65
	v_max_f32_e32 v64, v64, v64
	v_max_f32_e32 v64, v64, v65
	v_cmp_lt_f32_e32 vcc, s2, v64
	s_cmp_lg_u64 vcc, 0
	s_cselect_b64 s[2:3], -1, 0
	s_cbranch_vccnz .LBB1_163

.LBB1_114:
	s_add_i32 s14, s27, s31
	s_add_i32 s2, s26, s23
	s_add_i32 s3, s14, 2
	s_mov_b32 s51, s3
	s_cmp_lt_i32 s3, s50
	s_mov_b32 s3, m0
	s_mov_b32 m0, s2
	s_nop 0
	global_load_lds_dwordx4 v211, s[4:5]
	s_mov_b32 m0, s3
	s_cbranch_scc1 .LBB1_116
	s_cmp_gt_i32 s51, s50
	s_cbranch_scc1 .Lmfill_1a
	s_cmp_lg_u32 s52, 0
	s_cbranch_scc1 .Lpodd_1a
	s_nop 7
	s_nop 3
	v_add_u32_e32 v57, 0xffffff85, v65
	v_cmp_lt_i32_e64 s[54:55], v57, v207
	v_add_u32_e32 v58, 0xffffff85, v65
	v_cmp_le_i32_e64 s[56:57], v58, v207
	v_add_u32_e32 v57, 0xffffff87, v65
	v_cmp_le_i32_e64 s[58:59], v57, v207
	v_cndmask_b32_e64 v113, v252, v113, s[54:55]
	v_add_u32_e32 v58, 0xffffff88, v65
	v_cmp_le_i32_e64 s[54:55], v58, v207
	v_cndmask_b32_e64 v112, v252, v112, s[56:57]
	v_add_u32_e32 v57, 0xffffff8d, v65
	v_cmp_le_i32_e64 s[56:57], v57, v207
	v_cndmask_b32_e64 v114, v252, v114, s[58:59]
	v_add_u32_e32 v58, 0xffffff8e, v65
	v_cmp_le_i32_e64 s[58:59], v58, v207
	v_cndmask_b32_e64 v115, v252, v115, s[54:55]
	v_add_u32_e32 v57, 0xffffff8f, v65
	v_cmp_le_i32_e64 s[54:55], v57, v207
	v_cndmask_b32_e64 v116, v252, v116, s[56:57]
	v_add_u32_e32 v58, 0xffffff90, v65
	v_cmp_le_i32_e64 s[56:57], v58, v207
	v_cndmask_b32_e64 v117, v252, v117, s[58:59]
	v_add_u32_e32 v57, 0xffffff95, v65
	v_cmp_le_i32_e64 s[58:59], v57, v207
	v_cndmask_b32_e64 v118, v252, v118, s[54:55]
	v_add_u32_e32 v58, 0xffffff96, v65
	v_cmp_le_i32_e64 s[54:55], v58, v207
	v_cndmask_b32_e64 v119, v252, v119, s[56:57]
	v_add_u32_e32 v57, 0xffffff97, v65
	v_cmp_le_i32_e64 s[56:57], v57, v207
	v_cndmask_b32_e64 v120, v252, v120, s[58:59]
	v_add_u32_e32 v58, 0xffffff98, v65
	v_cmp_le_i32_e64 s[58:59], v58, v207
	v_cndmask_b32_e64 v121, v252, v121, s[54:55]
	v_add_u32_e32 v57, 0xffffff9d, v65
	v_cmp_le_i32_e64 s[54:55], v57, v207
	v_cndmask_b32_e64 v122, v252, v122, s[56:57]
	v_add_u32_e32 v58, 0xffffff9e, v65
	v_cmp_le_i32_e64 s[56:57], v58, v207
	v_cndmask_b32_e64 v123, v252, v123, s[58:59]
	v_add_u32_e32 v57, 0xffffff9f, v65
	v_cmp_le_i32_e64 s[58:59], v57, v207
	v_cndmask_b32_e64 v124, v252, v124, s[54:55]
	v_add_u32_e32 v58, 0xffffffa0, v65
	v_cmp_le_i32_e64 s[54:55], v58, v207
	v_cndmask_b32_e64 v125, v252, v125, s[56:57]
	v_cndmask_b32_e64 v126, v252, v126, s[58:59]
	v_cndmask_b32_e64 v127, v252, v127, s[54:55]
	v_mov_b32_e32 v96, v252
	v_mov_b32_e32 v97, v252
	v_mov_b32_e32 v98, v252
	v_mov_b32_e32 v99, v252
	v_mov_b32_e32 v100, v252
	v_mov_b32_e32 v101, v252
	v_mov_b32_e32 v102, v252
	v_mov_b32_e32 v103, v252
	v_mov_b32_e32 v104, v252
	v_mov_b32_e32 v105, v252
	v_mov_b32_e32 v106, v252
	v_mov_b32_e32 v107, v252
	v_mov_b32_e32 v108, v252
	v_mov_b32_e32 v109, v252
	v_mov_b32_e32 v110, v252
	v_mov_b32_e32 v111, v252
	s_branch .Lpend_1a
.Lpodd_1a:
	s_nop 7
	s_nop 3
	v_add_u32_e32 v57, 0xffffffa5, v65
	v_cmp_le_i32_e64 s[54:55], v57, v207
	v_add_u32_e32 v58, 0xffffffa6, v65
	v_cmp_le_i32_e64 s[56:57], v58, v207
	v_add_u32_e32 v57, 0xffffffa7, v65
	v_cmp_le_i32_e64 s[58:59], v57, v207
	v_cndmask_b32_e64 v96, v252, v96, s[54:55]
	v_add_u32_e32 v58, 0xffffffa8, v65
	v_cmp_le_i32_e64 s[54:55], v58, v207
	v_cndmask_b32_e64 v97, v252, v97, s[56:57]
	v_add_u32_e32 v57, 0xffffffad, v65
	v_cmp_le_i32_e64 s[56:57], v57, v207
	v_cndmask_b32_e64 v98, v252, v98, s[58:59]
	v_add_u32_e32 v58, 0xffffffae, v65
	v_cmp_le_i32_e64 s[58:59], v58, v207
	v_cndmask_b32_e64 v99, v252, v99, s[54:55]
	v_add_u32_e32 v57, 0xffffffaf, v65
	v_cmp_le_i32_e64 s[54:55], v57, v207
	v_cndmask_b32_e64 v100, v252, v100, s[56:57]
	v_add_u32_e32 v58, 0xffffffb0, v65
	v_cmp_le_i32_e64 s[56:57], v58, v207
	v_cndmask_b32_e64 v101, v252, v101, s[58:59]
	v_add_u32_e32 v57, 0xffffffb5, v65
	v_cmp_le_i32_e64 s[58:59], v57, v207
	v_cndmask_b32_e64 v102, v252, v102, s[54:55]
	v_add_u32_e32 v58, 0xffffffb6, v65
	v_cmp_le_i32_e64 s[54:55], v58, v207
	v_cndmask_b32_e64 v103, v252, v103, s[56:57]
	v_add_u32_e32 v57, 0xffffffb7, v65
	v_cmp_le_i32_e64 s[56:57], v57, v207
	v_cndmask_b32_e64 v104, v252, v104, s[58:59]
	v_add_u32_e32 v58, 0xffffffb8, v65
	v_cmp_le_i32_e64 s[58:59], v58, v207
	v_cndmask_b32_e64 v105, v252, v105, s[54:55]
	v_add_u32_e32 v57, 0xffffffbd, v65
	v_cmp_le_i32_e64 s[54:55], v57, v207
	v_cndmask_b32_e64 v106, v252, v106, s[56:57]
	v_add_u32_e32 v58, 0xffffffbe, v65
	v_cmp_le_i32_e64 s[56:57], v58, v207
	v_cndmask_b32_e64 v107, v252, v107, s[58:59]
	v_add_u32_e32 v57, 0xffffffbf, v65
	v_cmp_le_i32_e64 s[58:59], v57, v207
	v_cndmask_b32_e64 v108, v252, v108, s[54:55]
	v_subrev_u32_e32 v58, 64, v65
	v_cmp_le_i32_e64 s[54:55], v58, v207
	v_cndmask_b32_e64 v109, v252, v109, s[56:57]
	v_cndmask_b32_e64 v110, v252, v110, s[58:59]
	v_cndmask_b32_e64 v111, v252, v111, s[54:55]
.Lpend_1a:
.LBB1_116:
	v_add_f32_e32 v64, v64, v56
	v_max_f32_e32 v56, v113, v113
	v_max_f32_e32 v57, v112, v112
	v_max_f32_e32 v56, v57, v56
	v_max3_f32 v57, v114, v115, v97
	v_max3_f32 v56, v56, v96, v98
	v_max3_f32 v56, v56, v99, v116
	v_max3_f32 v57, v57, v118, v119
	v_max3_f32 v56, v56, v117, v100
	v_max3_f32 v57, v57, v102, v103
	v_max3_f32 v56, v56, v101, v120
	v_max3_f32 v57, v57, v122, v123
	v_max3_f32 v56, v56, v121, v104
	v_max3_f32 v57, v57, v106, v107
	v_max3_f32 v56, v56, v105, v124
	v_max3_f32 v57, v57, v126, v127
	v_max3_f32 v56, v56, v125, v108
	v_max3_f32 v57, v57, v110, v111
	v_max3_f32 v56, v56, v109, v57
	v_mov_b32_e32 v57, v56
	s_nop 1
	v_permlane32_swap_b32_e32 v56, v57
	v_max_f32_e32 v57, v57, v57
	v_max_f32_e32 v56, v56, v56
	v_max_f32_e32 v56, v56, v57
	v_cmp_lt_f32_e32 vcc, s30, v56
	s_cmp_lg_u64 vcc, 0
	s_cselect_b64 s[2:3], -1, 0
	s_cbranch_vccnz .LBB1_154

.LBB1_125:
	s_add_i32 s14, s14, 3
	s_cmp_lt_i32 s14, s50
	s_cbranch_scc1 .LBB1_127
	s_cmp_gt_i32 s14, s50
	s_cbranch_scc1 .Lmfill_1b
	s_cmp_lg_u32 s52, 0
	s_cbranch_scc1 .Lpodd_1b
	s_nop 7
	s_nop 3
	v_subrev_u32_e32 v96, 59, v65
	v_cmp_lt_u32_e64 s[54:55], v96, v207
	v_subrev_u32_e32 v97, 59, v65
	v_cmp_le_u32_e64 s[56:57], v97, v207
	v_subrev_u32_e32 v96, 57, v65
	v_cmp_le_u32_e64 s[58:59], v96, v207
	v_cndmask_b32_e64 v81, v252, v81, s[54:55]
	v_subrev_u32_e32 v97, 56, v65
	v_cmp_le_u32_e64 s[54:55], v97, v207
	v_cndmask_b32_e64 v80, v252, v80, s[56:57]
	v_subrev_u32_e32 v96, 51, v65
	v_cmp_le_u32_e64 s[56:57], v96, v207
	v_cndmask_b32_e64 v82, v252, v82, s[58:59]
	v_subrev_u32_e32 v97, 50, v65
	v_cmp_le_u32_e64 s[58:59], v97, v207
	v_cndmask_b32_e64 v83, v252, v83, s[54:55]
	v_subrev_u32_e32 v96, 49, v65
	v_cmp_le_u32_e64 s[54:55], v96, v207
	v_cndmask_b32_e64 v84, v252, v84, s[56:57]
	v_subrev_u32_e32 v97, 48, v65
	v_cmp_le_u32_e64 s[56:57], v97, v207
	v_cndmask_b32_e64 v85, v252, v85, s[58:59]
	v_subrev_u32_e32 v96, 43, v65
	v_cmp_le_u32_e64 s[58:59], v96, v207
	v_cndmask_b32_e64 v86, v252, v86, s[54:55]
	v_subrev_u32_e32 v97, 42, v65
	v_cmp_le_u32_e64 s[54:55], v97, v207
	v_cndmask_b32_e64 v87, v252, v87, s[56:57]
	v_subrev_u32_e32 v96, 41, v65
	v_cmp_le_u32_e64 s[56:57], v96, v207
	v_cndmask_b32_e64 v88, v252, v88, s[58:59]
	v_subrev_u32_e32 v97, 40, v65
	v_cmp_le_u32_e64 s[58:59], v97, v207
	v_cndmask_b32_e64 v89, v252, v89, s[54:55]
	v_subrev_u32_e32 v96, 35, v65
	v_cmp_le_u32_e64 s[54:55], v96, v207
	v_cndmask_b32_e64 v90, v252, v90, s[56:57]
	v_subrev_u32_e32 v97, 34, v65
	v_cmp_le_u32_e64 s[56:57], v97, v207
	v_cndmask_b32_e64 v91, v252, v91, s[58:59]
	v_subrev_u32_e32 v96, 33, v65
	v_cmp_le_u32_e64 s[58:59], v96, v207
	v_cndmask_b32_e64 v92, v252, v92, s[54:55]
	v_subrev_u32_e32 v97, 32, v65
	v_cmp_le_u32_e64 s[54:55], v97, v207
	v_cndmask_b32_e64 v93, v252, v93, s[56:57]
	v_cndmask_b32_e64 v94, v252, v94, s[58:59]
	v_cndmask_b32_e64 v95, v252, v95, s[54:55]
	v_mov_b32_e32 v48, v252
	v_mov_b32_e32 v49, v252
	v_mov_b32_e32 v50, v252
	v_mov_b32_e32 v51, v252
	v_mov_b32_e32 v52, v252
	v_mov_b32_e32 v53, v252
	v_mov_b32_e32 v54, v252
	v_mov_b32_e32 v55, v252
	v_mov_b32_e32 v56, v252
	v_mov_b32_e32 v57, v252
	v_mov_b32_e32 v58, v252
	v_mov_b32_e32 v59, v252
	v_mov_b32_e32 v60, v252
	v_mov_b32_e32 v61, v252
	v_mov_b32_e32 v62, v252
	v_mov_b32_e32 v63, v252
	s_branch .Lpend_1b
.Lpodd_1b:
	s_nop 7
	s_nop 3
	v_subrev_u32_e32 v96, 27, v65
	v_cmp_le_u32_e64 s[54:55], v96, v207
	v_subrev_u32_e32 v97, 26, v65
	v_cmp_le_u32_e64 s[56:57], v97, v207
	v_subrev_u32_e32 v96, 25, v65
	v_cmp_le_u32_e64 s[58:59], v96, v207
	v_cndmask_b32_e64 v48, v252, v48, s[54:55]
	v_subrev_u32_e32 v97, 24, v65
	v_cmp_le_u32_e64 s[54:55], v97, v207
	v_cndmask_b32_e64 v49, v252, v49, s[56:57]
	v_subrev_u32_e32 v96, 19, v65
	v_cmp_le_u32_e64 s[56:57], v96, v207
	v_cndmask_b32_e64 v50, v252, v50, s[58:59]
	v_subrev_u32_e32 v97, 18, v65
	v_cmp_le_u32_e64 s[58:59], v97, v207
	v_cndmask_b32_e64 v51, v252, v51, s[54:55]
	v_subrev_u32_e32 v96, 17, v65
	v_cmp_le_u32_e64 s[54:55], v96, v207
	v_cndmask_b32_e64 v52, v252, v52, s[56:57]
	v_add_u32_e32 v97, -16, v65
	v_cmp_le_u32_e64 s[56:57], v97, v207
	v_cndmask_b32_e64 v53, v252, v53, s[58:59]
	v_add_u32_e32 v96, -11, v65
	v_cmp_le_u32_e64 s[58:59], v96, v207
	v_cndmask_b32_e64 v54, v252, v54, s[54:55]
	v_add_u32_e32 v97, -10, v65
	v_cmp_le_u32_e64 s[54:55], v97, v207
	v_cndmask_b32_e64 v55, v252, v55, s[56:57]
	v_add_u32_e32 v96, -9, v65
	v_cmp_le_u32_e64 s[56:57], v96, v207
	v_cndmask_b32_e64 v56, v252, v56, s[58:59]
	v_add_u32_e32 v97, -8, v65
	v_cmp_le_u32_e64 s[58:59], v97, v207
	v_cndmask_b32_e64 v57, v252, v57, s[54:55]
	v_add_u32_e32 v96, -3, v65
	v_cmp_le_u32_e64 s[54:55], v96, v207
	v_cndmask_b32_e64 v58, v252, v58, s[56:57]
	v_add_u32_e32 v97, -2, v65
	v_cmp_le_u32_e64 s[56:57], v97, v207
	v_cndmask_b32_e64 v59, v252, v59, s[58:59]
	v_add_u32_e32 v96, -1, v65
	v_cmp_le_u32_e64 s[58:59], v96, v207
	v_cndmask_b32_e64 v60, v252, v60, s[54:55]
	v_cmp_le_u32_e64 s[54:55], v65, v207
	v_cndmask_b32_e64 v61, v252, v61, s[56:57]
	v_cndmask_b32_e64 v62, v252, v62, s[58:59]
	v_cndmask_b32_e64 v63, v252, v63, s[54:55]
.Lpend_1b:
.LBB1_127:
	v_add_f32_e32 v64, v64, v79
	v_max_f32_e32 v79, v81, v81
	v_max_f32_e32 v96, v80, v80
	v_max_f32_e32 v79, v96, v79
	v_max3_f32 v96, v82, v83, v49
	v_max3_f32 v79, v79, v48, v50
	v_max3_f32 v79, v79, v51, v84
	v_max3_f32 v96, v96, v86, v87
	v_max3_f32 v79, v79, v85, v52
	v_max3_f32 v96, v96, v54, v55
	v_max3_f32 v79, v79, v53, v88
	v_max3_f32 v96, v96, v90, v91
	v_max3_f32 v79, v79, v89, v56
	v_max3_f32 v96, v96, v58, v59
	v_max3_f32 v79, v79, v57, v92
	v_max3_f32 v96, v96, v94, v95
	v_max3_f32 v79, v79, v93, v60
	v_max3_f32 v96, v96, v62, v63
	v_max3_f32 v79, v79, v61, v96
	v_mov_b32_e32 v96, v79
	s_nop 1
	v_permlane32_swap_b32_e32 v79, v96
	v_max_f32_e32 v96, v96, v96
	v_max_f32_e32 v79, v79, v79
	v_max_f32_e32 v79, v79, v96
	v_cmp_lt_f32_e32 vcc, s30, v79
	s_cmp_lg_u64 vcc, 0
	s_cselect_b64 s[14:15], -1, 0
	s_cbranch_vccnz .LBB1_157
